# baseline (speedup 1.0000x reference)
_Z8dog_mainPKfS0_S0_S0_S0_S0_S0_Pf:
	s_load_dwordx8 s[12:19], s[0:1], 0x0
	s_load_dwordx8 s[20:27], s[0:1], 0x20
	s_and_b32 s3, s2, 7
	s_lshl_b32 s3, s3, 5
	s_lshr_b32 s4, s2, 3
	s_add_i32 s4, s3, s4
	s_and_b32 s6, s4, 3
	s_lshr_b32 s7, s4, 2
	s_mov_b32 s5, 0
	s_lshl_b64 s[8:9], s[4:5], 18
	v_and_b32_e32 v1, 63, v0
	v_lshrrev_b32_e32 v2, 6, v0
	v_and_b32_e32 v3, 15, v0
	v_and_b32_e32 v7, 31, v0
	v_lshl_or_b32 v5, v2, 5, v7
	v_lshlrev_b32_e32 v5, 2, v5
	v_mov_b32_e32 v4, v5
	v_lshlrev_b32_e32 v6, 4, v1
	v_lshl_or_b32 v6, v2, 12, v6
	v_bfe_u32 v7, v0, 4, 2
	v_readfirstlane_b32 s28, v2
	s_waitcnt lgkmcnt(0)
	global_load_dword v32, v4, s[18:19]
	global_load_dword v33, v4, s[20:21]
	global_load_dword v34, v4, s[22:23]
	global_load_dword v35, v4, s[24:25]
	global_load_dword v36, v4, s[14:15]
	global_load_dword v37, v4, s[16:17]
	s_add_u32 s12, s12, s8
	s_addc_u32 s13, s13, s9
	global_load_dwordx4 v[128:131], v6, s[12:13] offset:0 nt
	global_load_dwordx4 v[132:135], v6, s[12:13] offset:1024 nt
	global_load_dwordx4 v[136:139], v6, s[12:13] offset:2048 nt
	global_load_dwordx4 v[140:143], v6, s[12:13] offset:3072 nt
	v_add_u32_e32 v6, 0x8000, v6
	global_load_dwordx4 v[144:147], v6, s[12:13] offset:0 nt
	global_load_dwordx4 v[148:151], v6, s[12:13] offset:1024 nt
	global_load_dwordx4 v[152:155], v6, s[12:13] offset:2048 nt
	global_load_dwordx4 v[156:159], v6, s[12:13] offset:3072 nt
	s_cmp_ge_u32 s28, 4
	s_cbranch_scc0 .Lstag_skip
	s_sleep 4
